# phase 11 S5 chunk states: bid bits permuted so that an XCD owns the 4 groups g that share a 128-byte line of each token row
# speedup vs baseline: 1.0106x; 1.0106x over previous
; __device__ __forceinline__ void phase_qkprep_s5a(const Params& P, float* sm, int bid, int nb) {
;     ...
;         for (int item = wave * nb + bid; item < 64 * 9 * 2; item += nw) {
;             const int dg = item & 63, ph = (item >> 6) & 1, nt9 = item >> 7;
;             const int dir = dg >> 5, g = dg & 31;
;             const int c = nt9 * 32 + (lane & 31), cc = c < 260 ? c : 259;
;             f32x16 a0, a1;
; #pragma unroll
;             for (int q = 0; q < 16; ++q) { a0[q] = 0.f; a1[q] = 0.f; }
;             const bfr* e0 = S5E + ((size_t)dg * 4 + ph) * 64 * 512 + lane * 8;
;             const bfr* e1 = e0 + (size_t)2 * 64 * 512;
;             const bfr* ub = QK + 768 + g * 16 + (lane >> 5) * 8;
; #pragma unroll 8
;             for (int i = 0; i < 64; ++i) {
;                 const int row = s5_row(dir, cc * 64 + i);
;                 const bf16x8 bfrag = *(const bf16x8*)(ub + (size_t)row * 1280);
;                 const bf16x8 f0 = *(const bf16x8*)(e0 + (size_t)i * 512), f1 = *(const bf16x8*)(e1 + (size_t)i * 512);
;                 a0 = __builtin_amdgcn_mfma_f32_32x32x16_bf16(f0, bfrag, a0, 0, 0, 0);
;                 a1 = __builtin_amdgcn_mfma_f32_32x32x16_bf16(f1, bfrag, a1, 0, 0, 0);
;             }
.LBB0_1823:
	v_readlane_b32 s0, v253, 10
	s_barrier
	s_nop 0
	v_mul_lo_u32 v2, s0, v20
	s_cmpk_lg_u32 s0, 0x100
	s_mov_b32 s96, s44
	s_cbranch_scc1 .Ls5a_xcd
	s_and_b32 s96, s44, 0xe0
	s_and_b32 s97, s44, 7
	s_lshl_b32 s97, s97, 2
	s_or_b32 s96, s96, s97
	s_bfe_u32 s97, s44, 0x20003
	s_or_b32 s96, s96, s97
.Ls5a_xcd:
	v_add_u32_e32 v46, s96, v2
	s_movk_i32 s0, 0x480
	v_cmp_gt_i32_e32 vcc, s0, v46
	v_readlane_b32 s1, v253, 11
	s_and_saveexec_b64 s[4:5], vcc
	s_cbranch_execz .LBB0_1830
	v_lshrrev_b32_e32 v4, 5, v202
	v_lshlrev_b32_e32 v34, 4, v4
	v_mov_b32_e32 v35, 0
	v_lshl_add_u64 v[2:3], s[42:43], 0, v[34:35]
	s_mov_b64 s[0:1], 0x7078600
	s_add_u32 s6, s42, 0x3a112400
	v_lshl_add_u64 v[36:37], v[2:3], 0, s[0:1]
	v_lshlrev_b32_e32 v2, 2, v4
	v_lshlrev_b32_e32 v34, 4, v202
	s_addc_u32 s7, s43, 0
	v_lshl_add_u64 v[38:39], s[42:43], 0, v[34:35]
	s_mov_b64 s[8:9], 0
	s_movk_i32 s3, 0xff
	v_mov_b32_e32 v47, 0xff
	v_mov_b32_e32 v48, 0x41ff
	s_movk_i32 s12, 0xa00
	s_mov_b32 s13, 0x40766000
	s_mov_b32 s14, 0x40786000
	s_mov_b32 s15, 0x40767000
	s_mov_b32 s16, 0x40787000
	s_mov_b32 s17, 0x40768000
	s_mov_b32 s18, 0x40788000
	s_movk_i32 s19, 0x104
	v_lshlrev_b32_e32 v49, 3, v2
	s_movk_i32 s20, 0x47f
	v_mov_b32_e32 v50, v46
	s_branch .LBB0_1826
